# m32o3_1
# speedup vs baseline: 1.0357x; 1.0063x over previous
_Z10gae_kernelPKfPKiS2_S0_S0_S0_PfS3_:
	s_load_dwordx8 s[4:11], s[0:1], 0x0
	s_load_dwordx4 s[12:15], s[0:1], 0x20
	v_and_b32_e32 v64, 63, v0
	v_lshrrev_b32_e32 v1, 6, v0
	s_andn2_b32 s16, s2, 0xff
	s_and_b32 s17, s2, 7
	s_lshl_b32 s17, s17, 5
	s_bfe_u32 s18, s2, 0x50003
	s_or_b32 s16, s16, s17
	s_or_b32 s2, s16, s18
	s_mov_b32 s3, 0
	s_lshl_b64 s[2:3], s[2:3], 11
	v_lshlrev_b32_e32 v2, 9, v1
	v_lshlrev_b32_e32 v3, 2, v64
	v_or3_b32 v2, s2, v2, v3
	v_mov_b32_e32 v3, s3
	v_lshlrev_b64 v[18:19], 2, v[2:3]
	s_waitcnt lgkmcnt(0)
	v_lshl_add_u64 v[54:55], s[14:15], 0, v[18:19]
	v_lshl_add_u64 v[52:53], s[6:7], 0, v[18:19]
	global_load_dwordx4 v[10:13], v[54:55], off nt
	global_load_dwordx4 v[14:17], v[52:53], off nt
	v_lshl_add_u64 v[56:57], s[8:9], 0, v[18:19]
	global_load_dwordx4 v[20:23], v[56:57], off nt
	v_lshl_add_u64 v[58:59], s[12:13], 0, v[18:19]
	global_load_dwordx4 v[24:27], v[58:59], off nt
	v_lshl_add_u64 v[60:61], s[4:5], 0, v[18:19]
	global_load_dwordx4 v[28:31], v[60:61], off nt
	v_lshl_add_u64 v[62:63], s[10:11], 0, v[18:19]
	global_load_dwordx4 v[2:5], v[62:63], off nt
	global_load_dwordx4 v[32:35], v[60:61], off offset:1024 nt
	global_load_dwordx4 v[36:39], v[52:53], off offset:1024 nt
	global_load_dwordx4 v[40:43], v[56:57], off offset:1024 nt
	global_load_dwordx4 v[6:9], v[62:63], off offset:1024 nt
	global_load_dwordx4 v[44:47], v[58:59], off offset:1024 nt
	global_load_dwordx4 v[48:51], v[54:55], off offset:1024 nt
	v_mov_b32_e32 v66, 0
	v_mov_b32_e32 v68, 1.0
	v_mov_b32_e32 v69, 0
	v_mov_b32_e32 v70, 1.0
	v_mov_b32_e32 v71, 0
	v_mov_b32_e32 v72, 1.0
	v_bfe_u32 v73, v0, 4, 2
	v_cmp_gt_u32_e64 s[4:5], 16, v64
	v_mov_b32_e32 v65, 0
	v_mov_b32_e32 v67, 1.0
	s_waitcnt vmcnt(11)
	v_mul_f32_e32 v12, 0x3f7d70a4, v12
	s_waitcnt vmcnt(10)
	v_cmp_eq_u32_e32 vcc, 0, v14
	v_mul_f32_e32 v13, 0x3f7d70a4, v13
	v_mul_f32_e32 v10, 0x3f7d70a4, v10
	v_cndmask_b32_e64 v14, 0, 1.0, vcc
	s_waitcnt vmcnt(9)
	v_cmp_eq_u32_e32 vcc, 0, v20
	v_mul_f32_e32 v11, 0x3f7d70a4, v11
	s_waitcnt vmcnt(8)
	v_mul_f32_e32 v26, v26, v12
	v_cndmask_b32_e64 v20, 0, 1.0, vcc
	v_cmp_eq_u32_e32 vcc, 0, v15
	v_mul_f32_e32 v27, v27, v13
	v_mul_f32_e32 v24, v24, v10
	v_cndmask_b32_e64 v15, 0, 1.0, vcc
	v_cmp_eq_u32_e32 vcc, 0, v21
	v_mul_f32_e32 v25, v25, v11
	v_mul_f32_e32 v12, 0x3f733333, v12
	v_cndmask_b32_e64 v21, 0, 1.0, vcc
	v_cmp_eq_u32_e32 vcc, 0, v16
	v_mul_f32_e32 v13, 0x3f733333, v13
	v_mul_f32_e32 v10, 0x3f733333, v10
	v_cndmask_b32_e64 v16, 0, 1.0, vcc
	v_cmp_eq_u32_e32 vcc, 0, v22
	s_waitcnt vmcnt(7)
	v_fma_f32 v16, v26, v16, v30
	v_mul_f32_e32 v11, 0x3f733333, v11
	v_cndmask_b32_e64 v22, 0, 1.0, vcc
	v_cmp_eq_u32_e32 vcc, 0, v17
	v_fma_f32 v14, v24, v14, v28
	v_fma_f32 v15, v25, v15, v29
	v_cndmask_b32_e64 v17, 0, 1.0, vcc
	v_cmp_eq_u32_e32 vcc, 0, v23
	v_fmac_f32_e32 v31, v27, v17
	v_mul_f32_e32 v22, v12, v22
	v_cndmask_b32_e64 v23, 0, 1.0, vcc
	v_mul_f32_e32 v23, v13, v23
	s_waitcnt vmcnt(6)
	v_sub_f32_e32 v12, v16, v4
	v_sub_f32_e32 v13, v31, v5
	v_mul_f32_e32 v20, v10, v20
	v_mul_f32_e32 v21, v11, v21
	v_sub_f32_e32 v10, v14, v2
	v_sub_f32_e32 v11, v15, v3
	v_mul_f32_e32 v14, v23, v22
	v_fma_f32 v15, v22, v13, v12
	v_mul_f32_e32 v14, v14, v21
	v_fma_f32 v15, v21, v15, v11
	v_mul_f32_e32 v14, v14, v20
	v_fma_f32 v24, v20, v15, v10
	v_mov_b32_e32 v16, 1.0
	v_mov_b32_dpp v68, v14 row_shl:1 row_mask:0xf bank_mask:0xf
	v_mov_b32_dpp v66, v24 row_shl:1 row_mask:0xf bank_mask:0xf
	v_mul_f32_e32 v15, v14, v68
	v_fmac_f32_e32 v24, v14, v66
	v_cmp_eq_u32_e32 vcc, 2, v73
	v_mov_b32_dpp v70, v15 row_shl:2 row_mask:0xf bank_mask:0xf
	v_mov_b32_dpp v69, v24 row_shl:2 row_mask:0xf bank_mask:0xf
	v_mul_f32_e32 v14, v15, v70
	v_fmac_f32_e32 v24, v15, v69
	v_mov_b32_e32 v15, 0
	v_mov_b32_dpp v72, v14 row_shl:4 row_mask:0xf bank_mask:0xf
	v_mov_b32_dpp v71, v24 row_shl:4 row_mask:0xf bank_mask:0xf
	v_fmac_f32_e32 v24, v14, v71
	v_mul_f32_e32 v14, v14, v72
	s_nop 0
	v_mov_b32_dpp v15, v24 row_shl:8 row_mask:0xf bank_mask:0xf
	v_mov_b32_dpp v16, v14 row_shl:8 row_mask:0xf bank_mask:0xf
	v_fmac_f32_e32 v24, v14, v15
	v_mul_f32_e32 v14, v14, v16
	v_readlane_b32 s9, v24, 32
	v_readlane_b32 s2, v14, 48
	v_readlane_b32 s8, v14, 32
	v_readlane_b32 s6, v14, 16
	v_mov_b32_e32 v15, s2
	v_mul_f32_e32 v16, s8, v15
	v_cndmask_b32_e32 v15, 1.0, v15, vcc
	v_cmp_eq_u32_e64 s[2:3], 1, v73
	v_readlane_b32 s10, v24, 48
	v_mul_f32_e32 v17, s6, v16
	v_cndmask_b32_e64 v15, v15, v16, s[2:3]
	v_readlane_b32 s7, v24, 16
	v_cndmask_b32_e64 v15, v15, v17, s[4:5]
	v_mov_b32_e32 v16, s9
	v_mov_b32_e32 v17, s10
	v_fmac_f32_e32 v16, s8, v17
	v_mov_b32_e32 v25, s7
	v_cndmask_b32_e32 v17, 0, v17, vcc
	v_fmac_f32_e32 v25, s6, v16
	v_cndmask_b32_e64 v16, v17, v16, s[2:3]
	v_cndmask_b32_e64 v16, v16, v25, s[4:5]
	s_waitcnt vmcnt(4)
	v_cmp_eq_u32_e64 s[6:7], 0, v36
	v_fmac_f32_e32 v24, v14, v16
	v_mul_f32_e32 v28, v14, v15
	s_waitcnt vmcnt(0)
	v_mul_f32_e32 v15, 0x3f7d70a4, v48
	v_cndmask_b32_e64 v14, 0, 1.0, s[6:7]
	v_cmp_eq_u32_e64 s[6:7], 0, v40
	v_mul_f32_e32 v17, v44, v15
	v_mul_f32_e32 v15, 0x3f733333, v15
	v_cndmask_b32_e64 v16, 0, 1.0, s[6:7]
	v_cmp_eq_u32_e64 s[6:7], 0, v37
	v_mul_f32_e32 v25, v15, v16
	v_mul_f32_e32 v16, 0x3f7d70a4, v49
	v_cndmask_b32_e64 v15, 0, 1.0, s[6:7]
	v_cmp_eq_u32_e64 s[6:7], 0, v41
	v_fma_f32 v14, v17, v14, v32
	v_mul_f32_e32 v26, v45, v16
	v_cndmask_b32_e64 v17, 0, 1.0, s[6:7]
	v_mul_f32_e32 v16, 0x3f733333, v16
	v_fma_f32 v15, v26, v15, v33
	v_mul_f32_e32 v26, v16, v17
	v_mul_f32_e32 v17, 0x3f7d70a4, v50
	v_cmp_eq_u32_e64 s[6:7], 0, v38
	v_mul_f32_e32 v29, v46, v17
	v_mul_f32_e32 v17, 0x3f733333, v17
	v_cndmask_b32_e64 v16, 0, 1.0, s[6:7]
	v_cmp_eq_u32_e64 s[6:7], 0, v42
	v_fma_f32 v16, v29, v16, v34
	v_mul_f32_e32 v29, 0x3f7d70a4, v51
	v_cndmask_b32_e64 v27, 0, 1.0, s[6:7]
	v_cmp_eq_u32_e64 s[6:7], 0, v39
	v_mul_f32_e32 v27, v17, v27
	v_mul_f32_e32 v31, v47, v29
	v_cndmask_b32_e64 v17, 0, 1.0, s[6:7]
	v_cmp_eq_u32_e64 s[6:7], 0, v43
	v_fmac_f32_e32 v35, v31, v17
	v_mul_f32_e32 v29, 0x3f733333, v29
	v_cndmask_b32_e64 v30, 0, 1.0, s[6:7]
	v_sub_f32_e32 v16, v16, v8
	v_sub_f32_e32 v17, v35, v9
	v_mul_f32_e32 v29, v29, v30
	v_sub_f32_e32 v15, v15, v7
	v_fma_f32 v30, v27, v17, v16
	v_mul_f32_e32 v31, v29, v27
	v_sub_f32_e32 v14, v14, v6
	v_fma_f32 v30, v26, v30, v15
	v_mul_f32_e32 v31, v31, v26
	v_fma_f32 v30, v25, v30, v14
	v_mul_f32_e32 v31, v31, v25
	v_mov_b32_e32 v32, 0
	v_mov_b32_e32 v33, 1.0
	s_nop 0
	v_mov_b32_dpp v32, v30 row_shl:1 row_mask:0xf bank_mask:0xf
	v_mov_b32_dpp v33, v31 row_shl:1 row_mask:0xf bank_mask:0xf
	v_fmac_f32_e32 v30, v31, v32
	v_mul_f32_e32 v31, v31, v33
	v_mov_b32_e32 v32, 0
	v_mov_b32_e32 v33, 1.0
	s_nop 0
	v_mov_b32_dpp v32, v30 row_shl:2 row_mask:0xf bank_mask:0xf
	v_mov_b32_dpp v33, v31 row_shl:2 row_mask:0xf bank_mask:0xf
	v_fmac_f32_e32 v30, v31, v32
	v_mul_f32_e32 v31, v31, v33
	v_mov_b32_e32 v32, 0
	v_mov_b32_e32 v33, 1.0
	s_nop 0
	v_mov_b32_dpp v32, v30 row_shl:4 row_mask:0xf bank_mask:0xf
	v_mov_b32_dpp v33, v31 row_shl:4 row_mask:0xf bank_mask:0xf
	v_fmac_f32_e32 v30, v31, v32
	v_mul_f32_e32 v31, v31, v33
	s_nop 0
	v_mov_b32_dpp v65, v30 row_shl:8 row_mask:0xf bank_mask:0xf
	v_mov_b32_dpp v67, v31 row_shl:8 row_mask:0xf bank_mask:0xf
	v_fmac_f32_e32 v30, v31, v65
	v_mul_f32_e32 v31, v31, v67
	v_readlane_b32 s9, v30, 32
	v_readlane_b32 s10, v31, 48
	v_readlane_b32 s8, v31, 32
	v_readlane_b32 s6, v31, 16
	v_mov_b32_e32 v32, s10
	v_mul_f32_e32 v33, s8, v32
	v_cndmask_b32_e32 v32, 1.0, v32, vcc
	v_readlane_b32 s11, v30, 48
	v_mul_f32_e32 v34, s6, v33
	v_cndmask_b32_e64 v32, v32, v33, s[2:3]
	v_readlane_b32 s7, v30, 16
	v_cndmask_b32_e64 v32, v32, v34, s[4:5]
	v_mov_b32_e32 v33, s9
	v_mov_b32_e32 v34, s11
	v_fmac_f32_e32 v33, s8, v34
	v_mov_b32_e32 v35, s7
	v_cndmask_b32_e32 v34, 0, v34, vcc
	v_fmac_f32_e32 v35, s6, v33
	v_cndmask_b32_e64 v33, v34, v33, s[2:3]
	v_cndmask_b32_e64 v33, v33, v35, s[4:5]
	v_fmac_f32_e32 v30, v31, v33
	v_mul_f32_e32 v31, v31, v32
	v_readlane_b32 s6, v28, 0
	v_readlane_b32 s7, v24, 0
	v_readlane_b32 s4, v31, 0
	v_readlane_b32 s5, v30, 0
	v_cmp_eq_u32_e32 vcc, 0, v64
	s_and_saveexec_b64 s[2:3], vcc
	s_cbranch_execz .LBB0_4
	v_mov_b32_e32 v32, s4
	v_mov_b32_e32 v33, s7
	v_mov_b32_e32 v34, s5
	v_mul_f32_e32 v32, s6, v32
	v_lshlrev_b32_e32 v1, 2, v1
	v_fmac_f32_e32 v33, s6, v34
	ds_write2_b32 v1, v32, v33 offset1:4
